# speedup vs baseline: 1.0566x; 1.0055x over previous
_Z11prep_kernelPKfS0_S0_PcPfS2_S2_S2_:
	s_load_dwordx16 s[16:31], s[0:1], 0x0
	s_and_b32 s4, s2, 7
	s_lshr_b32 s5, s2, 3
	s_lshl_b32 s6, s4, 4
	s_add_u32 s6, s6, s5
	s_mul_i32 s7, s4, 48
	s_add_u32 s7, s7, s5
	s_add_u32 s7, s7, 0x70
	s_cmp_lt_u32 s5, 16
	s_cselect_b32 s8, s6, s7
	s_lshl_b32 s9, s8, 15
	v_lshrrev_b32_e32 v1, 6, v0
	v_and_b32_e32 v58, 63, v0
	v_lshlrev_b32_e32 v60, 4, v58
	v_readfirstlane_b32 s15, v1
	v_and_b32_e32 v63, 7, v58
	v_lshrrev_b32_e32 v62, 3, v58
	s_lshl_b32 s3, s15, 11
	s_add_u32 s9, s9, s3
	s_waitcnt lgkmcnt(0)
	s_sub_u32 s10, s9, 0x800000
	s_add_u32 s12, s20, s10
	s_addc_u32 s13, s21, 0
	s_mov_b32 s14, 4.0
	s_cmp_lt_u32 s8, 0x100
	s_cbranch_scc0 .Lpp_src
	s_sub_u32 s10, s9, 0x400000
	s_add_u32 s12, s18, s10
	s_addc_u32 s13, s19, 0
	s_cmp_lt_u32 s8, 0x80
	s_cbranch_scc0 .Lpp_src
	s_add_u32 s12, s16, s9
	s_addc_u32 s13, s17, 0
	s_mov_b32 s14, 0x4066d4ca
.Lpp_src:
	global_load_dwordx4 v[2:5], v60, s[12:13] nt
	global_load_dwordx4 v[6:9], v60, s[12:13] offset:1024 nt
	s_cmp_lg_u32 s15, 0
	s_cbranch_scc1 .Lpp_z1
	v_mov_b32_e32 v11, 0
	v_lshlrev_b32_e32 v10, 2, v0
	s_lshl_b32 s10, s8, 6
	s_add_u32 s10, s28, s10
	s_addc_u32 s11, s29, 0
	v_cmp_gt_u32_e32 vcc, 16, v0
	s_and_saveexec_b64 s[6:7], vcc
	global_store_dword v10, v11, s[10:11]
	s_mov_b64 exec, s[6:7]
.Lpp_z1:
	s_cmp_lg_u32 s15, 1
	s_cbranch_scc1 .Lpp_z2
	s_cmp_gt_u32 s8, 1
	s_cbranch_scc1 .Lpp_z2
	v_mov_b32_e32 v11, 0
	s_cmp_eq_u32 s8, 0
	s_cbranch_scc0 .Lpp_zout
	v_lshlrev_b32_e32 v10, 2, v58
	s_add_u32 s10, s28, 0x8000
	s_addc_u32 s11, s29, 0
	global_store_dword v10, v11, s[10:11]
	s_branch .Lpp_z2
.Lpp_zout:
	v_cmp_eq_u32_e32 vcc, 0, v58
	s_and_saveexec_b64 s[6:7], vcc
	global_store_dword v11, v11, s[30:31]
	s_mov_b64 exec, s[6:7]
.Lpp_z2:
	v_xor_b32_e32 v59, 16, v58
	v_lshlrev_b32_e32 v59, 2, v59
	v_xor_b32_e32 v61, 32, v58
	v_lshlrev_b32_e32 v61, 2, v61
	s_mul_i32 s3, s15, 0x900
	v_mul_u32_u24_e32 v57, 0x90, v62
	v_lshl_add_u32 v57, v63, 4, v57
	v_add_u32_e32 v57, s3, v57
	v_mul_u32_u24_e32 v56, 0x480, v62
	v_mul_u32_u24_e32 v55, 0x90, v63
	v_add3_u32 v56, v56, v55, s3
	s_lshl_b32 s6, s15, 1
	v_lshrrev_b32_e32 v55, 1, v63
	v_and_b32_e32 v54, 1, v63
	v_lshlrev_b32_e32 v55, 11, v55
	v_lshl_or_b32 v55, v54, 9, v55
	v_add_u32_e32 v54, s6, v62
	v_lshl_or_b32 v55, v54, 4, v55
	v_mov_b32_e32 v52, 1.0
	s_lshl_b32 s6, s8, 13
	s_add_u32 s10, s22, s6
	s_addc_u32 s11, s23, 0
	s_waitcnt vmcnt(1)
	v_pk_mul_f32 v[10:11], v[2:3], v[2:3]
	v_pk_fma_f32 v[10:11], v[4:5], v[4:5], v[10:11]
	s_waitcnt vmcnt(0)
	v_pk_mul_f32 v[12:13], v[6:7], v[6:7]
	v_pk_fma_f32 v[12:13], v[8:9], v[8:9], v[12:13]
	v_add_f32_e32 v10, v10, v11
	v_add_f32_e32 v12, v12, v13
	s_nop 1
	v_add_f32_dpp v10, v10, v10 quad_perm:[1,0,3,2] row_mask:0xf bank_mask:0xf bound_ctrl:1
	v_add_f32_dpp v12, v12, v12 quad_perm:[1,0,3,2] row_mask:0xf bank_mask:0xf bound_ctrl:1
	s_nop 1
	v_add_f32_dpp v10, v10, v10 quad_perm:[2,3,0,1] row_mask:0xf bank_mask:0xf bound_ctrl:1
	v_add_f32_dpp v12, v12, v12 quad_perm:[2,3,0,1] row_mask:0xf bank_mask:0xf bound_ctrl:1
	s_nop 1
	v_add_f32_dpp v10, v10, v10 row_half_mirror row_mask:0xf bank_mask:0xf bound_ctrl:1
	v_add_f32_dpp v12, v12, v12 row_half_mirror row_mask:0xf bank_mask:0xf bound_ctrl:1
	s_nop 1
	v_add_f32_dpp v10, v10, v10 row_mirror row_mask:0xf bank_mask:0xf bound_ctrl:1
	v_add_f32_dpp v12, v12, v12 row_mirror row_mask:0xf bank_mask:0xf bound_ctrl:1
	ds_bpermute_b32 v11, v59, v10
	ds_bpermute_b32 v13, v59, v12
	s_waitcnt lgkmcnt(1)
	v_add_f32_e32 v10, v10, v11
	s_waitcnt lgkmcnt(0)
	v_add_f32_e32 v12, v12, v13
	ds_bpermute_b32 v11, v61, v10
	ds_bpermute_b32 v13, v61, v12
	s_waitcnt lgkmcnt(1)
	v_add_f32_e32 v10, v10, v11
	s_waitcnt lgkmcnt(0)
	v_add_f32_e32 v12, v12, v13
	v_rsq_f32_e32 v10, v10
	v_rsq_f32_e32 v12, v12
	s_nop 0
	v_min_f32_e32 v10, 0x4cbebc20, v10
	v_min_f32_e32 v12, 0x4cbebc20, v12
	v_mul_f32_e32 v10, s14, v10
	v_mul_f32_e32 v12, s14, v12
	v_pk_mul_f32 v[2:3], v[2:3], v[10:11] op_sel_hi:[1,0]
	v_pk_mul_f32 v[4:5], v[4:5], v[10:11] op_sel_hi:[1,0]
	v_pk_mul_f32 v[6:7], v[6:7], v[12:13] op_sel_hi:[1,0]
	v_pk_mul_f32 v[8:9], v[8:9], v[12:13] op_sel_hi:[1,0]
	ds_write_b128 v57, v[2:5]
	ds_write_b128 v57, v[6:9] offset:1152
	s_nop 1
	v_pk_add_f32 v[2:3], v[2:3], v[6:7]
	v_pk_add_f32 v[4:5], v[4:5], v[8:9]
	s_mov_b64 exec, 0xffff
	ds_read_b128 v[12:15], v56
	ds_read_b128 v[16:19], v56 offset:16
	ds_read_b128 v[20:23], v56 offset:32
	ds_read_b128 v[24:27], v56 offset:48
	ds_read_b128 v[28:31], v56 offset:64
	ds_read_b128 v[32:35], v56 offset:80
	ds_read_b128 v[36:39], v56 offset:96
	ds_read_b128 v[40:43], v56 offset:112
	v_mov_b32_e32 v50, 0
	v_mov_b32_e32 v51, 0
	s_waitcnt lgkmcnt(0)
	v_cvt_scalef32_2xpk16_fp6_f32 v[44:49], v[12:27], v[28:43], v52
	s_nop 1
	global_store_dwordx4 v55, v[44:47], s[10:11]
	global_store_dwordx4 v55, v[48:51], s[10:11] offset:1024
	s_mov_b64 exec, -1
	s_cmp_lt_u32 s8, 0x100
	s_cbranch_scc0 .Lpp_end
	v_add_u32_e32 v10, s3, v60
	ds_write_b128 v10, v[2:5]
	s_waitcnt lgkmcnt(0)
	s_barrier
	s_sub_u32 s6, s15, 8
	s_cmp_gt_u32 s6, 3
	s_cbranch_scc1 .Lpp_end
	s_lshl_b32 s6, s6, 8
	v_lshl_add_u32 v10, v58, 2, s6
	ds_read_b32 v12, v10
	ds_read_b32 v13, v10 offset:2304
	ds_read_b32 v14, v10 offset:4608
	ds_read_b32 v15, v10 offset:6912
	ds_read_b32 v16, v10 offset:9216
	ds_read_b32 v17, v10 offset:11520
	ds_read_b32 v18, v10 offset:13824
	ds_read_b32 v19, v10 offset:16128
	ds_read_b32 v20, v10 offset:18432
	ds_read_b32 v21, v10 offset:20736
	ds_read_b32 v22, v10 offset:23040
	ds_read_b32 v23, v10 offset:25344
	ds_read_b32 v24, v10 offset:27648
	ds_read_b32 v25, v10 offset:29952
	ds_read_b32 v26, v10 offset:32256
	ds_read_b32 v27, v10 offset:34560
	s_cmp_lt_u32 s8, 0x80
	s_cselect_b32 s10, s24, s26
	s_cselect_b32 s11, s25, s27
	s_and_b32 s6, s8, 0x7f
	s_lshl_b32 s6, s6, 10
	s_add_u32 s10, s10, s6
	s_addc_u32 s11, s11, 0
	s_waitcnt lgkmcnt(14)
	v_add_f32_e32 v12, v12, v13
	s_waitcnt lgkmcnt(13)
	v_add_f32_e32 v12, v12, v14
	s_waitcnt lgkmcnt(12)
	v_add_f32_e32 v12, v12, v15
	s_waitcnt lgkmcnt(11)
	v_add_f32_e32 v12, v12, v16
	s_waitcnt lgkmcnt(10)
	v_add_f32_e32 v12, v12, v17
	s_waitcnt lgkmcnt(9)
	v_add_f32_e32 v12, v12, v18
	s_waitcnt lgkmcnt(8)
	v_add_f32_e32 v12, v12, v19
	s_waitcnt lgkmcnt(7)
	v_add_f32_e32 v12, v12, v20
	s_waitcnt lgkmcnt(6)
	v_add_f32_e32 v12, v12, v21
	s_waitcnt lgkmcnt(5)
	v_add_f32_e32 v12, v12, v22
	s_waitcnt lgkmcnt(4)
	v_add_f32_e32 v12, v12, v23
	s_waitcnt lgkmcnt(3)
	v_add_f32_e32 v12, v12, v24
	s_waitcnt lgkmcnt(2)
	v_add_f32_e32 v12, v12, v25
	s_waitcnt lgkmcnt(1)
	v_add_f32_e32 v12, v12, v26
	s_waitcnt lgkmcnt(0)
	v_add_f32_e32 v12, v12, v27
	global_store_dword v10, v12, s[10:11]

	.amdhsa_kernel _Z11prep_kernelPKfS0_S0_PcPfS2_S2_S2_
		.amdhsa_group_segment_fixed_size 36864
		.amdhsa_private_segment_fixed_size 0
		.amdhsa_kernarg_size 64
		.amdhsa_user_sgpr_count 2
		.amdhsa_user_sgpr_dispatch_ptr 0
		.amdhsa_user_sgpr_queue_ptr 0
		.amdhsa_user_sgpr_kernarg_segment_ptr 1
		.amdhsa_user_sgpr_dispatch_id 0
		.amdhsa_user_sgpr_kernarg_preload_length 0
		.amdhsa_user_sgpr_kernarg_preload_offset 0
		.amdhsa_user_sgpr_private_segment_size 0
		.amdhsa_uses_dynamic_stack 0
		.amdhsa_enable_private_segment 0
		.amdhsa_system_sgpr_workgroup_id_x 1
		.amdhsa_system_sgpr_workgroup_id_y 0
		.amdhsa_system_sgpr_workgroup_id_z 0
		.amdhsa_system_sgpr_workgroup_info 0
		.amdhsa_system_vgpr_workitem_id 0
		.amdhsa_next_free_vgpr 64
		.amdhsa_next_free_sgpr 32
		.amdhsa_accum_offset 64
		.amdhsa_reserve_vcc 1
		.amdhsa_float_round_mode_32 0
		.amdhsa_float_round_mode_16_64 0
		.amdhsa_float_denorm_mode_32 3
		.amdhsa_float_denorm_mode_16_64 3
		.amdhsa_dx10_clamp 1
		.amdhsa_ieee_mode 1
		.amdhsa_fp16_overflow 0
		.amdhsa_tg_split 0
		.amdhsa_exception_fp_ieee_invalid_op 0
		.amdhsa_exception_fp_denorm_src 0
		.amdhsa_exception_fp_ieee_div_zero 0
		.amdhsa_exception_fp_ieee_overflow 0
		.amdhsa_exception_fp_ieee_underflow 0
		.amdhsa_exception_fp_ieee_inexact 0
		.amdhsa_exception_int_div_zero 0
	.end_amdhsa_kernel

.LBB2_2:
	s_or_b64 exec, exec, s[4:5]
	v_cmp_gt_u32_e32 vcc, 16, v0
	s_waitcnt lgkmcnt(0)
	s_barrier
	s_and_saveexec_b64 s[4:5], vcc
	s_cbranch_execz .LBB2_8
	v_lshlrev_b32_e32 v1, 2, v0
	ds_read2_b32 v[6:7], v1 offset1:16
	v_add_u32_e32 v14, 0x400, v1
	ds_read2_b32 v[8:9], v14 offset1:16
	ds_read2_b32 v[10:11], v1 offset0:32 offset1:48
	ds_read2_b32 v[12:13], v14 offset0:32 offset1:48
	v_cmp_eq_u32_e32 vcc, 0, v0
	s_waitcnt lgkmcnt(2)
	v_add_f32_e32 v8, 0, v8
	v_add_f32_e32 v6, 0, v6
	v_add_f32_e32 v6, v6, v7
	s_waitcnt lgkmcnt(1)
	v_add_f32_e32 v10, v6, v10
	ds_read2_b32 v[6:7], v1 offset0:64 offset1:80
	v_add_f32_e32 v8, v8, v9
	s_waitcnt lgkmcnt(1)
	v_add_f32_e32 v12, v8, v12
	ds_read2_b32 v[8:9], v14 offset0:64 offset1:80
	v_add_f32_e32 v10, v10, v11
	s_waitcnt lgkmcnt(1)
	v_add_f32_e32 v6, v10, v6
	ds_read2_b32 v[10:11], v1 offset0:96 offset1:112
	v_add_f32_e32 v12, v12, v13
	s_waitcnt lgkmcnt(1)
	v_add_f32_e32 v8, v12, v8
	ds_read2_b32 v[12:13], v14 offset0:96 offset1:112
	v_add_f32_e32 v6, v6, v7
	s_waitcnt lgkmcnt(1)
	v_add_f32_e32 v10, v6, v10
	ds_read2_b32 v[6:7], v1 offset0:128 offset1:144
	v_add_f32_e32 v8, v8, v9
	s_waitcnt lgkmcnt(1)
	v_add_f32_e32 v12, v8, v12
	ds_read2_b32 v[8:9], v14 offset0:128 offset1:144
	v_add_f32_e32 v10, v10, v11
	s_waitcnt lgkmcnt(1)
	v_add_f32_e32 v6, v10, v6
	ds_read2_b32 v[10:11], v1 offset0:160 offset1:176
	v_add_f32_e32 v12, v12, v13
	s_waitcnt lgkmcnt(1)
	v_add_f32_e32 v8, v12, v8
	ds_read2_b32 v[12:13], v14 offset0:160 offset1:176
	v_add_f32_e32 v6, v6, v7
	v_add_f32_e32 v8, v8, v9
	s_waitcnt lgkmcnt(1)
	v_add_f32_e32 v9, v6, v10
	ds_read2_b32 v[6:7], v1 offset0:192 offset1:208
	s_waitcnt lgkmcnt(1)
	v_add_f32_e32 v10, v8, v12
	v_add_f32_e32 v11, v9, v11
	ds_read2_b32 v[8:9], v14 offset0:192 offset1:208
	v_add_f32_e32 v15, v10, v13
	s_waitcnt lgkmcnt(1)
	v_add_f32_e32 v6, v11, v6
	ds_read2_b32 v[10:11], v1 offset0:224 offset1:240
	ds_read2_b32 v[12:13], v14 offset0:224 offset1:240
	v_add_f32_e32 v6, v6, v7
	s_waitcnt lgkmcnt(2)
	v_add_f32_e32 v1, v15, v8
	v_add_f32_e32 v1, v1, v9
	s_waitcnt lgkmcnt(1)
	v_add_f32_e32 v6, v6, v10
	s_waitcnt lgkmcnt(0)
	v_add_f32_e32 v1, v1, v12
	v_add_f32_e32 v6, v6, v11
	v_add_f32_e32 v1, v1, v13
	v_mul_f32_e32 v7, v6, v1
	ds_bpermute_b32 v4, v4, v7
	s_waitcnt lgkmcnt(0)
	v_fmac_f32_e32 v4, v6, v1
	ds_bpermute_b32 v1, v3, v4
	s_waitcnt lgkmcnt(0)
	v_add_f32_e32 v1, v4, v1
	ds_bpermute_b32 v2, v2, v1
	s_waitcnt lgkmcnt(0)
	v_add_f32_e32 v1, v1, v2
	ds_bpermute_b32 v2, v5, v1
	s_and_b64 exec, exec, vcc
	s_cbranch_execz .LBB2_8
	v_mov_b32_e32 v0, 0
	ds_read_b128 v[4:7], v0 offset:2048
	s_waitcnt lgkmcnt(1)
	v_add_f32_e32 v0, v1, v2
	v_mul_f32_e32 v0, 0.5, v0
	v_mul_f32_e32 v0, 0xb18df4e0, v0
	s_cmp_eq_u32 s2, 0
	s_waitcnt lgkmcnt(0)
	v_add_f32_e32 v1, v4, v5
	v_add_f32_e32 v1, v1, v6
	v_add_f32_e32 v1, v1, v7
	v_fmamk_f32 v0, v1, 0x39800000, v0
	v_add_f32_e32 v1, 0.5, v0
	s_cselect_b64 vcc, -1, 0
	s_mov_b64 s[4:5], exec
	v_cndmask_b32_e32 v1, v0, v1, vcc
	v_bfrev_b32_e32 v0, 1

amdhsa.kernels:
  - .agpr_count:     0
    .args:
      - .actual_access:  read_only
        .address_space:  global
        .offset:         0
        .size:           8
        .value_kind:     global_buffer
      - .actual_access:  read_only
        .address_space:  global
        .offset:         8
        .size:           8
        .value_kind:     global_buffer
      - .actual_access:  read_only
        .address_space:  global
        .offset:         16
        .size:           8
        .value_kind:     global_buffer
      - .actual_access:  write_only
        .address_space:  global
        .offset:         24
        .size:           8
        .value_kind:     global_buffer
      - .actual_access:  write_only
        .address_space:  global
        .offset:         32
        .size:           8
        .value_kind:     global_buffer
      - .actual_access:  write_only
        .address_space:  global
        .offset:         40
        .size:           8
        .value_kind:     global_buffer
      - .actual_access:  write_only
        .address_space:  global
        .offset:         48
        .size:           8
        .value_kind:     global_buffer
      - .actual_access:  write_only
        .address_space:  global
        .offset:         56
        .size:           8
        .value_kind:     global_buffer
    .group_segment_fixed_size: 36864
    .kernarg_segment_align: 8
    .kernarg_segment_size: 64
    .language:       OpenCL C
    .language_version:
      - 2
      - 0
    .max_flat_workgroup_size: 1024
    .name:           _Z11prep_kernelPKfS0_S0_PcPfS2_S2_S2_
    .private_segment_fixed_size: 0
    .sgpr_count:     38
    .sgpr_spill_count: 0
    .symbol:         _Z11prep_kernelPKfS0_S0_PcPfS2_S2_S2_.kd
    .uniform_work_group_size: 1
    .uses_dynamic_stack: false
    .vgpr_count:     64
    .vgpr_spill_count: 0
    .wavefront_size: 64
  - .agpr_count:     0
    .args:
      - .address_space:  global
        .offset:         0
        .size:           8
        .value_kind:     global_buffer
      - .address_space:  global
        .offset:         8
        .size:           8
        .value_kind:     global_buffer
      - .address_space:  global
        .offset:         16
        .size:           8
        .value_kind:     global_buffer
    .group_segment_fixed_size: 65536
    .kernarg_segment_align: 8
    .kernarg_segment_size: 24
    .language:       OpenCL C
    .language_version:
      - 2
      - 0
    .max_flat_workgroup_size: 512
    .name:           _Z11main_kernelPKcPfS1_
    .private_segment_fixed_size: 0
    .sgpr_count:     34
    .sgpr_spill_count: 0
    .symbol:         _Z11main_kernelPKcPfS1_.kd
    .uniform_work_group_size: 1
    .uses_dynamic_stack: false
    .vgpr_count:     128
    .vgpr_spill_count: 0
    .wavefront_size: 64
  - .agpr_count:     0
    .args:
      - .actual_access:  read_only
        .address_space:  global
        .offset:         0
        .size:           8
        .value_kind:     global_buffer
      - .actual_access:  read_only
        .address_space:  global
        .offset:         8
        .size:           8
        .value_kind:     global_buffer
      - .actual_access:  read_only
        .address_space:  global
        .offset:         16
        .size:           8
        .value_kind:     global_buffer
      - .actual_access:  read_only
        .address_space:  global
        .offset:         24
        .size:           8
        .value_kind:     global_buffer
      - .address_space:  global
        .offset:         32
        .size:           8
        .value_kind:     global_buffer
    .group_segment_fixed_size: 2064
    .kernarg_segment_align: 8
    .kernarg_segment_size: 40
    .language:       OpenCL C
    .language_version:
      - 2
      - 0
    .max_flat_workgroup_size: 256
    .name:           _Z12final_kernelPKfS0_S0_S0_Pf
    .private_segment_fixed_size: 0
    .sgpr_count:     18
    .sgpr_spill_count: 0
    .symbol:         _Z12final_kernelPKfS0_S0_S0_Pf.kd
    .uniform_work_group_size: 1
    .uses_dynamic_stack: false
    .vgpr_count:     35
    .vgpr_spill_count: 0
    .wavefront_size: 64
